# MoE weight conversion split: 36864 items beside the selected attention
# speedup vs baseline: 1.0186x; 1.0017x over previous
.LBB0_995:
	s_cmp_lg_u32 s89, 0
	s_cbranch_scc1 .LBB0_1002
	s_andn2_b64 vcc, exec, s[10:11]
	s_cbranch_vccnz .LBB0_1002
	s_sub_i32 s0, s82, s15
	s_lshl_b32 s25, s0, 3
	s_add_i32 s25, s25, s92
	s_cmpk_gt_u32 s25, 0x8fff
	s_cbranch_scc1 .LBB0_1002
	s_sub_i32 s0, s88, s15
	s_lshl_b32 s8, s0, 3
	s_add_u32 s9, s86, 0x50000000
	s_mul_i32 s0, s92, 0x4100
	s_addc_u32 s10, s87, 0
	s_load_dwordx2 s[4:5], s[90:91], 0xa0
	s_load_dwordx2 s[6:7], s[90:91], 0xb0
	s_add_i32 s2, s0, 0
	s_lshl_b32 s0, s25, 6
	s_lshl_b32 s1, s25, 5
	s_and_b32 s1, s1, 0x780
	s_and_b32 s0, s0, 64
	v_lshlrev_b32_e32 v0, 2, v1
	s_or_b32 s0, s1, s0
	s_waitcnt vmcnt(3)
	v_and_b32_e32 v142, 60, v0
	v_or_b32_e32 v0, s0, v142
	v_readlane_b32 s0, v255, 4
	s_bitcmp0_b32 s0, 7
	s_waitcnt lgkmcnt(0)
	s_cselect_b32 s1, s5, s7
	s_cselect_b32 s0, s4, s6
	s_lshl_b32 s3, s25, 13
	s_and_b32 s3, s3, 0x1f000000
	s_add_u32 s0, s0, s3
	s_addc_u32 s1, s1, 0
	s_and_b32 s3, s25, 0x7c0
	v_lshrrev_b32_e32 v143, 4, v1
	s_waitcnt vmcnt(0)
	v_or_b32_e32 v4, s3, v143
	v_lshlrev_b32_e32 v130, 2, v0
	v_mov_b32_e32 v131, 0
	v_lshl_add_u64 v[2:3], s[0:1], 0, v[130:131]
	v_lshlrev_b32_e32 v130, 13, v4
	v_lshl_add_u64 v[2:3], v[2:3], 0, v[130:131]
	s_mov_b32 s11, 0x8000
	v_add_co_u32_e32 v4, vcc, s11, v2
	s_mov_b32 s12, 0x10000
	s_nop 0
	v_addc_co_u32_e32 v5, vcc, 0, v3, vcc
	global_load_dwordx4 v[66:69], v[2:3], off nt
	global_load_dwordx4 v[70:73], v[4:5], off nt
	v_add_co_u32_e32 v4, vcc, s12, v2
	s_mov_b32 s13, 0x18000
	s_nop 0
	v_addc_co_u32_e32 v5, vcc, 0, v3, vcc
	v_add_co_u32_e32 v6, vcc, s13, v2
	s_mov_b32 s14, 0x20000
	s_nop 0
	v_addc_co_u32_e32 v7, vcc, 0, v3, vcc
	global_load_dwordx4 v[74:77], v[4:5], off nt
	global_load_dwordx4 v[78:81], v[6:7], off nt
	v_add_co_u32_e32 v4, vcc, s14, v2
	s_mov_b32 s16, 0x28000
	s_nop 0
	v_addc_co_u32_e32 v5, vcc, 0, v3, vcc
	v_add_co_u32_e32 v6, vcc, s16, v2
	s_mov_b32 s17, 0x30000
	s_nop 0
	v_addc_co_u32_e32 v7, vcc, 0, v3, vcc
	global_load_dwordx4 v[82:85], v[4:5], off nt
	global_load_dwordx4 v[86:89], v[6:7], off nt
	v_add_co_u32_e32 v4, vcc, s17, v2
	s_mov_b32 s18, 0x38000
	s_nop 0
	v_addc_co_u32_e32 v5, vcc, 0, v3, vcc
	v_add_co_u32_e32 v6, vcc, s18, v2
	s_mov_b32 s19, 0x40000
	s_nop 0
	v_addc_co_u32_e32 v7, vcc, 0, v3, vcc
	global_load_dwordx4 v[90:93], v[4:5], off nt
	global_load_dwordx4 v[94:97], v[6:7], off nt
	v_add_co_u32_e32 v4, vcc, s19, v2
	s_mov_b32 s20, 0x48000
	s_nop 0
	v_addc_co_u32_e32 v5, vcc, 0, v3, vcc
	v_add_co_u32_e32 v6, vcc, s20, v2
	s_mov_b32 s21, 0x50000
	s_nop 0
	v_addc_co_u32_e32 v7, vcc, 0, v3, vcc
	global_load_dwordx4 v[98:101], v[4:5], off nt
	global_load_dwordx4 v[102:105], v[6:7], off nt
	v_add_co_u32_e32 v4, vcc, s21, v2
	s_mov_b32 s22, 0x58000
	s_nop 0
	v_addc_co_u32_e32 v5, vcc, 0, v3, vcc
	v_add_co_u32_e32 v6, vcc, s22, v2
	s_mov_b32 s0, 0x60000
	s_nop 0
	v_addc_co_u32_e32 v7, vcc, 0, v3, vcc
	global_load_dwordx4 v[106:109], v[4:5], off nt
	global_load_dwordx4 v[110:113], v[6:7], off nt
	v_add_co_u32_e32 v4, vcc, s0, v2
	s_mov_b32 s0, 0x68000
	s_nop 0
	v_addc_co_u32_e32 v5, vcc, 0, v3, vcc
	v_add_co_u32_e32 v6, vcc, s0, v2
	s_mov_b32 s0, 0x70000
	s_nop 0
	v_addc_co_u32_e32 v7, vcc, 0, v3, vcc
	global_load_dwordx4 v[114:117], v[4:5], off nt
	global_load_dwordx4 v[118:121], v[6:7], off nt
	v_add_co_u32_e32 v4, vcc, s0, v2
	s_mov_b32 s0, 0x78000
	s_nop 0
	v_addc_co_u32_e32 v5, vcc, 0, v3, vcc
	v_add_co_u32_e32 v2, vcc, s0, v2
	s_lshl_b32 s0, s15, 3
	s_nop 0
	v_addc_co_u32_e32 v3, vcc, 0, v3, vcc
	global_load_dwordx4 v[122:125], v[4:5], off nt
	global_load_dwordx4 v[126:129], v[2:3], off nt
	s_sub_i32 s23, 0, s0
	s_lshl_b32 s0, s82, 3
	v_lshlrev_b32_e32 v3, 4, v1
	s_add_i32 s24, s92, s0
	s_lshl_b32 s0, s88, 7
	s_lshl_b32 s1, s15, 7
	v_and_b32_e32 v132, 48, v3
	s_sub_i32 s26, s0, s1
	s_lshl_b32 s0, s88, 3
	s_lshl_b32 s1, s15, 4
	v_mul_u32_u24_e32 v3, 0x104, v132
	v_and_b32_e32 v4, 60, v1
	s_sub_i32 s27, s0, s1
	s_add_i32 s0, s24, s0
	v_add3_u32 v144, s2, v3, v4
	v_lshlrev_b32_e32 v3, 5, v1
	s_sub_i32 s0, s0, s1
	v_lshl_add_u32 v0, v142, 2, s2
	v_mul_u32_u24_e32 v2, 0x104, v143
	v_and_b32_e32 v134, 0x780, v3
	s_lshl_b32 s28, s0, 6
	s_lshl_b32 s0, s88, 9
	s_lshl_b32 s1, s15, 9
	v_mov_b32_e32 v133, v131
	v_mov_b32_e32 v135, v131
	v_or_b32_e32 v136, 0x800, v134
	v_mov_b32_e32 v137, v131
	v_or_b32_e32 v138, 0x1000, v134
	v_mov_b32_e32 v139, v131
	v_or_b32_e32 v140, 0x1800, v134
	v_mov_b32_e32 v141, v131
	s_lshl_b32 s25, s25, 4
	s_sub_i32 s15, s0, s1
	v_add_u32_e32 v145, v0, v2
	s_branch .LBB0_1000
.LBB0_999:
	v_add_u32_e32 v0, 0x410, v145
	s_waitcnt vmcnt(31)
	ds_write2_b32 v145, v66, v67 offset1:1
	ds_write2_b32 v145, v68, v69 offset0:2 offset1:3
	s_waitcnt vmcnt(30)
	ds_write2_b32 v0, v70, v71 offset1:1
	v_add_u32_e32 v0, 0x418, v145
	ds_write2_b32 v0, v72, v73 offset1:1
	v_add_u32_e32 v0, 0x820, v145
	s_waitcnt vmcnt(29)
	ds_write2_b32 v0, v74, v75 offset1:1
	v_add_u32_e32 v0, 0x828, v145
	ds_write2_b32 v0, v76, v77 offset1:1
	v_add_u32_e32 v0, 0xc30, v145
	s_waitcnt vmcnt(28)
	ds_write2_b32 v0, v78, v79 offset1:1
	v_add_u32_e32 v0, 0xc38, v145
	ds_write2_b32 v0, v80, v81 offset1:1
	v_add_u32_e32 v0, 0x1040, v145
	s_waitcnt vmcnt(27)
	ds_write2_b32 v0, v82, v83 offset1:1
	v_add_u32_e32 v0, 0x1048, v145
	ds_write2_b32 v0, v84, v85 offset1:1
	v_add_u32_e32 v0, 0x1450, v145
	s_waitcnt vmcnt(26)
	ds_write2_b32 v0, v86, v87 offset1:1
	v_add_u32_e32 v0, 0x1458, v145
	ds_write2_b32 v0, v88, v89 offset1:1
	v_add_u32_e32 v0, 0x1860, v145
	s_waitcnt vmcnt(25)
	ds_write2_b32 v0, v90, v91 offset1:1
	v_add_u32_e32 v0, 0x1868, v145
	ds_write2_b32 v0, v92, v93 offset1:1
	v_add_u32_e32 v0, 0x1c70, v145
	s_waitcnt vmcnt(24)
	ds_write2_b32 v0, v94, v95 offset1:1
	v_add_u32_e32 v0, 0x1c78, v145
	ds_write2_b32 v0, v96, v97 offset1:1
	v_add_u32_e32 v0, 0x2080, v145
	s_waitcnt vmcnt(23)
	ds_write2_b32 v0, v98, v99 offset1:1
	v_add_u32_e32 v0, 0x2088, v145
	ds_write2_b32 v0, v100, v101 offset1:1
	v_add_u32_e32 v0, 0x2490, v145
	s_waitcnt vmcnt(22)
	ds_write2_b32 v0, v102, v103 offset1:1
	v_add_u32_e32 v0, 0x2498, v145
	ds_write2_b32 v0, v104, v105 offset1:1
	v_add_u32_e32 v0, 0x28a0, v145
	s_waitcnt vmcnt(21)
	ds_write2_b32 v0, v106, v107 offset1:1
	v_add_u32_e32 v0, 0x28a8, v145
	ds_write2_b32 v0, v108, v109 offset1:1
	v_add_u32_e32 v0, 0x2cb0, v145
	s_waitcnt vmcnt(20)
	ds_write2_b32 v0, v110, v111 offset1:1
	v_add_u32_e32 v0, 0x2cb8, v145
	ds_write2_b32 v0, v112, v113 offset1:1
	v_add_u32_e32 v0, 0x30c0, v145
	s_waitcnt vmcnt(19)
	ds_write2_b32 v0, v114, v115 offset1:1
	v_add_u32_e32 v0, 0x30c8, v145
	ds_write2_b32 v0, v116, v117 offset1:1
	v_add_u32_e32 v0, 0x34d0, v145
	s_waitcnt vmcnt(18)
	ds_write2_b32 v0, v118, v119 offset1:1
	v_add_u32_e32 v0, 0x34d8, v145
	ds_write2_b32 v0, v120, v121 offset1:1
	v_add_u32_e32 v0, 0x38e0, v145
	s_waitcnt vmcnt(17)
	ds_write2_b32 v0, v122, v123 offset1:1
	v_add_u32_e32 v0, 0x38e8, v145
	ds_write2_b32 v0, v124, v125 offset1:1
	v_add_u32_e32 v0, 0x3cf0, v145
	s_waitcnt vmcnt(16)
	ds_write2_b32 v0, v126, v127 offset1:1
	v_add_u32_e32 v0, 0x3cf8, v145
	ds_write2_b32 v0, v128, v129 offset1:1
	s_waitcnt lgkmcnt(0)
	ds_read2_b32 v[70:71], v144 offset1:16
	ds_read2_b32 v[72:73], v144 offset0:65 offset1:81
	ds_read2_b32 v[74:75], v144 offset0:130 offset1:146
	ds_read2_b32 v[76:77], v144 offset0:195 offset1:211
	v_mov_b32_e32 v66, 0
	s_waitcnt lgkmcnt(3)
	v_mul_f32_e32 v0, 0x43800000, v70
	s_waitcnt lgkmcnt(2)
	v_mul_f32_e32 v67, 0x43800000, v72
	v_cvt_pk_fp8_f32 v66, v0, v67
	v_add_u32_e32 v0, 0x400, v144
	ds_read2_b32 v[78:79], v0 offset0:4 offset1:20
	ds_read2_b32 v[80:81], v0 offset0:69 offset1:85
	ds_read2_b32 v[82:83], v0 offset0:134 offset1:150
	s_waitcnt lgkmcnt(4)
	v_mul_f32_e32 v68, 0x43800000, v74
	s_waitcnt lgkmcnt(3)
	v_mul_f32_e32 v67, 0x43800000, v76
	ds_read2_b32 v[84:85], v0 offset0:199 offset1:215
	v_add_u32_e32 v106, 0x800, v144
	v_cvt_pk_fp8_f32 v66, v68, v67 op_sel:[0,0,1]
	s_waitcnt lgkmcnt(3)
	v_mul_f32_e32 v68, 0x43800000, v78
	s_waitcnt lgkmcnt(2)
	v_mul_f32_e32 v69, 0x43800000, v80
	v_mov_b32_e32 v67, 0
	ds_read2_b32 v[86:87], v106 offset0:8 offset1:24
	ds_read2_b32 v[88:89], v106 offset0:73 offset1:89
	v_add_u32_e32 v107, 0xc00, v144
	v_cvt_pk_fp8_f32 v67, v68, v69
	ds_read2_b32 v[90:91], v106 offset0:138 offset1:154
	ds_read2_b32 v[92:93], v106 offset0:203 offset1:219
	ds_read2_b32 v[94:95], v107 offset0:12 offset1:28
	ds_read2_b32 v[96:97], v107 offset0:77 offset1:93
	s_ashr_i32 s0, s29, 11
	s_ashr_i32 s1, s0, 31
	s_lshl_b64 s[0:1], s[0:1], 23
	s_waitcnt lgkmcnt(7)
	v_mul_f32_e32 v70, 0x43800000, v82
	s_waitcnt lgkmcnt(6)
	v_mul_f32_e32 v68, 0x43800000, v84
	s_add_u32 s0, s9, s0
	v_cvt_pk_fp8_f32 v67, v70, v68 op_sel:[0,0,1]
	s_waitcnt lgkmcnt(5)
	v_mul_f32_e32 v69, 0x43800000, v86
	s_waitcnt lgkmcnt(4)
	v_mul_f32_e32 v70, 0x43800000, v88
	v_mov_b32_e32 v68, 0
	ds_read2_b32 v[98:99], v107 offset0:142 offset1:158
	ds_read2_b32 v[100:101], v107 offset0:207 offset1:223
	s_addc_u32 s1, s10, s1
	s_and_b32 s2, s25, 0x3f0
	s_bfe_u32 s3, s29, 0x40007
	v_cvt_pk_fp8_f32 v68, v69, v70
	s_waitcnt lgkmcnt(3)
	v_mul_f32_e32 v70, 0x43800000, v94
	s_waitcnt lgkmcnt(2)
	v_mul_f32_e32 v76, 0x43800000, v96
	v_mov_b32_e32 v69, 0
	s_or_b32 s2, s2, s3
	v_cvt_pk_fp8_f32 v69, v70, v76
	s_lshl_b32 s2, s2, 13
	s_add_u32 s0, s0, s2
	v_mul_f32_e32 v72, 0x43800000, v90
	v_mul_f32_e32 v74, 0x43800000, v92
	s_addc_u32 s1, s1, 0
	s_and_b32 s2, s29, 64
	v_cvt_pk_fp8_f32 v68, v72, v74 op_sel:[0,0,1]
	s_waitcnt lgkmcnt(1)
	v_mul_f32_e32 v70, 0x43800000, v98
	s_waitcnt lgkmcnt(0)
	v_mul_f32_e32 v72, 0x43800000, v100
	s_add_u32 s0, s0, s2
	v_cvt_pk_fp8_f32 v69, v70, v72 op_sel:[0,0,1]
	s_addc_u32 s1, s1, 0
	v_lshl_add_u64 v[102:103], s[0:1], 0, v[132:133]
	v_lshl_add_u64 v[104:105], v[102:103], 0, v[134:135]
	global_store_dwordx4 v[104:105], v[66:69], off nt
	v_mul_f32_e32 v70, 0x43800000, v77
	v_mul_f32_e32 v72, 0x43800000, v93
	v_mul_f32_e32 v67, 0x43800000, v71
	v_mul_f32_e32 v68, 0x43800000, v73
	v_mov_b32_e32 v66, 0
	v_cvt_pk_fp8_f32 v66, v67, v68
	v_mul_f32_e32 v68, 0x43800000, v79
	v_mul_f32_e32 v71, 0x43800000, v81
	v_mov_b32_e32 v67, 0
	v_cvt_pk_fp8_f32 v67, v68, v71
	v_mul_f32_e32 v69, 0x43800000, v75
	v_cvt_pk_fp8_f32 v66, v69, v70 op_sel:[0,0,1]
	v_mul_f32_e32 v68, 0x43800000, v83
	v_mul_f32_e32 v69, 0x43800000, v85
	v_cvt_pk_fp8_f32 v67, v68, v69 op_sel:[0,0,1]
	v_mul_f32_e32 v69, 0x43800000, v87
	v_mul_f32_e32 v70, 0x43800000, v89
	v_mov_b32_e32 v68, 0
	v_cvt_pk_fp8_f32 v68, v69, v70
	v_mul_f32_e32 v70, 0x43800000, v95
	v_mul_f32_e32 v73, 0x43800000, v97
	v_mov_b32_e32 v69, 0
	v_cvt_pk_fp8_f32 v69, v70, v73
	v_mul_f32_e32 v71, 0x43800000, v91
	v_cvt_pk_fp8_f32 v68, v71, v72 op_sel:[0,0,1]
	v_mul_f32_e32 v70, 0x43800000, v99
	v_mul_f32_e32 v71, 0x43800000, v101
	v_cvt_pk_fp8_f32 v69, v70, v71 op_sel:[0,0,1]
	ds_read2_b32 v[70:71], v144 offset0:32 offset1:48
	ds_read2_b32 v[72:73], v144 offset0:97 offset1:113
	ds_read2_b32 v[74:75], v144 offset0:162 offset1:178
	v_lshl_add_u64 v[76:77], v[102:103], 0, v[136:137]
	s_add_i32 s24, s24, s8
	global_store_dwordx4 v[76:77], v[66:69], off nt
	ds_read2_b32 v[76:77], v144 offset0:227 offset1:243
	ds_read2_b32 v[78:79], v0 offset0:36 offset1:52
	ds_read2_b32 v[80:81], v0 offset0:101 offset1:117
	s_waitcnt lgkmcnt(5)
	v_mul_f32_e32 v67, 0x43800000, v70
	s_waitcnt lgkmcnt(4)
	v_mul_f32_e32 v68, 0x43800000, v72
	v_mov_b32_e32 v66, 0
	v_cvt_pk_fp8_f32 v66, v67, v68
	s_waitcnt lgkmcnt(3)
	v_mul_f32_e32 v69, 0x43800000, v74
	s_waitcnt lgkmcnt(2)
	v_mul_f32_e32 v67, 0x43800000, v76
	ds_read2_b32 v[82:83], v0 offset0:166 offset1:182
	ds_read2_b32 v[84:85], v0 offset0:231 offset1:247
	v_cvt_pk_fp8_f32 v66, v69, v67 op_sel:[0,0,1]
	s_waitcnt lgkmcnt(3)
	v_mul_f32_e32 v68, 0x43800000, v78
	s_waitcnt lgkmcnt(2)
	v_mul_f32_e32 v69, 0x43800000, v80
	v_mov_b32_e32 v67, 0
	ds_read2_b32 v[86:87], v106 offset0:40 offset1:56
	v_cvt_pk_fp8_f32 v67, v68, v69
	ds_read2_b32 v[88:89], v106 offset0:105 offset1:121
	ds_read2_b32 v[90:91], v106 offset0:170 offset1:186
	ds_read2_b32 v[92:93], v106 offset0:235 offset1:251
	ds_read2_b32 v[94:95], v107 offset0:44 offset1:60
	ds_read2_b32 v[96:97], v107 offset0:109 offset1:125
	s_waitcnt lgkmcnt(7)
	v_mul_f32_e32 v0, 0x43800000, v82
	s_waitcnt lgkmcnt(6)
	v_mul_f32_e32 v68, 0x43800000, v84
	v_cvt_pk_fp8_f32 v67, v0, v68 op_sel:[0,0,1]
	s_waitcnt lgkmcnt(5)
	v_mul_f32_e32 v0, 0x43800000, v86
	s_waitcnt lgkmcnt(4)
	v_mul_f32_e32 v69, 0x43800000, v88
	v_mov_b32_e32 v68, 0
	ds_read2_b32 v[98:99], v107 offset0:174 offset1:190
	ds_read2_b32 v[100:101], v107 offset0:239 offset1:255
	v_cvt_pk_fp8_f32 v68, v0, v69
	s_waitcnt lgkmcnt(3)
	v_mul_f32_e32 v0, 0x43800000, v94
	s_waitcnt lgkmcnt(2)
	v_mul_f32_e32 v74, 0x43800000, v96
	v_mov_b32_e32 v69, 0
	v_cvt_pk_fp8_f32 v69, v0, v74
	v_mul_f32_e32 v70, 0x43800000, v90
	v_mul_f32_e32 v72, 0x43800000, v92
	v_cvt_pk_fp8_f32 v68, v70, v72 op_sel:[0,0,1]
	s_waitcnt lgkmcnt(1)
	v_mul_f32_e32 v0, 0x43800000, v98
	s_waitcnt lgkmcnt(0)
	v_mul_f32_e32 v70, 0x43800000, v100
	v_cvt_pk_fp8_f32 v69, v0, v70 op_sel:[0,0,1]
	v_mul_f32_e32 v0, 0x43800000, v71
	v_mul_f32_e32 v71, 0x43800000, v73
	v_mov_b32_e32 v70, 0
	v_cvt_pk_fp8_f32 v70, v0, v71
	v_mul_f32_e32 v0, 0x43800000, v79
	v_mul_f32_e32 v74, 0x43800000, v81
	v_mov_b32_e32 v71, 0
	v_cvt_pk_fp8_f32 v71, v0, v74
	v_mul_f32_e32 v72, 0x43800000, v75
	v_mul_f32_e32 v73, 0x43800000, v77
	v_cvt_pk_fp8_f32 v70, v72, v73 op_sel:[0,0,1]
	v_mul_f32_e32 v0, 0x43800000, v83
	v_mul_f32_e32 v72, 0x43800000, v85
	v_cvt_pk_fp8_f32 v71, v0, v72 op_sel:[0,0,1]
	v_mul_f32_e32 v0, 0x43800000, v87
	v_mul_f32_e32 v73, 0x43800000, v89
	v_mov_b32_e32 v72, 0
	v_cvt_pk_fp8_f32 v72, v0, v73
	v_mul_f32_e32 v0, 0x43800000, v95
	v_mul_f32_e32 v76, 0x43800000, v97
	v_mov_b32_e32 v73, 0
	v_cvt_pk_fp8_f32 v73, v0, v76
	v_mul_f32_e32 v74, 0x43800000, v91
	v_mul_f32_e32 v75, 0x43800000, v93
	v_cvt_pk_fp8_f32 v72, v74, v75 op_sel:[0,0,1]
	v_mul_f32_e32 v0, 0x43800000, v99
	v_mul_f32_e32 v74, 0x43800000, v101
	v_cvt_pk_fp8_f32 v73, v0, v74 op_sel:[0,0,1]
	v_lshl_add_u64 v[74:75], v[102:103], 0, v[138:139]
	global_store_dwordx4 v[74:75], v[66:69], off nt
	s_add_i32 s0, s23, s24
	s_add_i32 s25, s25, s26
	v_lshl_add_u64 v[66:67], v[102:103], 0, v[140:141]
	global_store_dwordx4 v[66:67], v[70:73], off nt
	s_waitcnt lgkmcnt(0)
	s_add_i32 s28, s28, s15
	s_waitcnt vmcnt(4)
	v_mov_b64_e32 v[68:69], v[4:5]
	v_mov_b64_e32 v[72:73], v[8:9]
	v_mov_b64_e32 v[76:77], v[12:13]
	v_mov_b64_e32 v[80:81], v[16:17]
	v_mov_b64_e32 v[84:85], v[20:21]
	v_mov_b64_e32 v[88:89], v[24:25]
	v_mov_b64_e32 v[92:93], v[28:29]
	v_mov_b64_e32 v[96:97], v[32:33]
	v_mov_b64_e32 v[100:101], v[36:37]
	v_mov_b64_e32 v[104:105], v[40:41]
	v_mov_b64_e32 v[108:109], v[44:45]
	v_mov_b64_e32 v[112:113], v[48:49]
	v_mov_b64_e32 v[116:117], v[52:53]
	v_mov_b64_e32 v[120:121], v[56:57]
	v_mov_b64_e32 v[124:125], v[60:61]
	v_mov_b64_e32 v[128:129], v[64:65]
	s_cmp_lt_i32 s0, 0x9000
	v_mov_b64_e32 v[66:67], v[2:3]
	v_mov_b64_e32 v[70:71], v[6:7]
	v_mov_b64_e32 v[74:75], v[10:11]
	v_mov_b64_e32 v[78:79], v[14:15]
	v_mov_b64_e32 v[82:83], v[18:19]
	v_mov_b64_e32 v[86:87], v[22:23]
	v_mov_b64_e32 v[90:91], v[26:27]
	v_mov_b64_e32 v[94:95], v[30:31]
	v_mov_b64_e32 v[98:99], v[34:35]
	v_mov_b64_e32 v[102:103], v[38:39]
	v_mov_b64_e32 v[106:107], v[42:43]
	v_mov_b64_e32 v[110:111], v[46:47]
	v_mov_b64_e32 v[114:115], v[50:51]
	v_mov_b64_e32 v[118:119], v[54:55]
	v_mov_b64_e32 v[122:123], v[58:59]
	v_mov_b64_e32 v[126:127], v[62:63]
	s_cbranch_scc0 .LBB0_1002
.LBB0_1000:
	s_add_i32 s29, s23, s24
	s_add_i32 s30, s27, s24
	s_cmp_gt_i32 s30, 0x8fff
	s_cbranch_scc1 .Lcv4_last
	s_lshr_b32 s1, s28, 1
	s_ashr_i32 s0, s30, 11
	s_and_b32 s2, s1, 0x780
	s_and_b32 s3, s28, 64
	s_bitcmp0_b32 s29, 1
	s_cselect_b32 s31, s5, s7
	s_cselect_b32 s33, s4, s6
	s_ashr_i32 s1, s0, 31
	s_lshl_b64 s[0:1], s[0:1], 24
	s_add_u32 s0, s33, s0
	s_addc_u32 s1, s31, s1
	s_or_b32 s2, s3, s2
	v_or_b32_e32 v0, s2, v142
	s_and_b32 s2, s30, 0x7c0
	v_or_b32_e32 v4, s2, v143
	v_lshlrev_b32_e32 v130, 2, v0
	v_lshl_add_u64 v[2:3], s[0:1], 0, v[130:131]
	v_lshlrev_b32_e32 v130, 13, v4
	v_lshl_add_u64 v[58:59], v[2:3], 0, v[130:131]
	v_add_co_u32_e32 v10, vcc, s11, v58
	s_nop 1
	v_addc_co_u32_e32 v11, vcc, 0, v59, vcc
	global_load_dwordx4 v[2:5], v[58:59], off nt
	global_load_dwordx4 v[6:9], v[10:11], off nt
	v_add_co_u32_e32 v10, vcc, s12, v58
	s_nop 1
	v_addc_co_u32_e32 v11, vcc, 0, v59, vcc
	v_add_co_u32_e32 v14, vcc, s13, v58
	s_nop 1
	v_addc_co_u32_e32 v15, vcc, 0, v59, vcc
	v_add_co_u32_e32 v18, vcc, s14, v58
	global_load_dwordx4 v[10:13], v[10:11], off nt
	s_nop 0
	global_load_dwordx4 v[14:17], v[14:15], off nt
	v_addc_co_u32_e32 v19, vcc, 0, v59, vcc
	v_add_co_u32_e32 v22, vcc, s16, v58
	s_nop 1
	v_addc_co_u32_e32 v23, vcc, 0, v59, vcc
	v_add_co_u32_e32 v26, vcc, s17, v58
	global_load_dwordx4 v[18:21], v[18:19], off nt
	s_nop 0
	global_load_dwordx4 v[22:25], v[22:23], off nt
	v_addc_co_u32_e32 v27, vcc, 0, v59, vcc
	v_add_co_u32_e32 v30, vcc, s18, v58
	s_nop 1
	v_addc_co_u32_e32 v31, vcc, 0, v59, vcc
	v_add_co_u32_e32 v34, vcc, s19, v58
	global_load_dwordx4 v[26:29], v[26:27], off nt
	s_nop 0
	global_load_dwordx4 v[30:33], v[30:31], off nt
	v_addc_co_u32_e32 v35, vcc, 0, v59, vcc
	v_add_co_u32_e32 v38, vcc, s20, v58
	s_nop 1
	v_addc_co_u32_e32 v39, vcc, 0, v59, vcc
	v_add_co_u32_e32 v42, vcc, s21, v58
	global_load_dwordx4 v[34:37], v[34:35], off nt
	s_nop 0
	global_load_dwordx4 v[38:41], v[38:39], off nt
	v_addc_co_u32_e32 v43, vcc, 0, v59, vcc
	v_add_co_u32_e32 v46, vcc, s22, v58
	s_nop 1
	v_addc_co_u32_e32 v47, vcc, 0, v59, vcc
	v_add_co_u32_e32 v50, vcc, 0x60000, v58
	global_load_dwordx4 v[42:45], v[42:43], off nt
	s_nop 0
	global_load_dwordx4 v[46:49], v[46:47], off nt
	v_addc_co_u32_e32 v51, vcc, 0, v59, vcc
	v_add_co_u32_e32 v54, vcc, 0x68000, v58
	s_nop 1
	v_addc_co_u32_e32 v55, vcc, 0, v59, vcc
	v_add_co_u32_e32 v60, vcc, 0x70000, v58
	global_load_dwordx4 v[50:53], v[50:51], off nt
	s_nop 0
	global_load_dwordx4 v[54:57], v[54:55], off nt
	v_addc_co_u32_e32 v61, vcc, 0, v59, vcc
	v_add_co_u32_e32 v62, vcc, 0x78000, v58
	s_nop 1
	v_addc_co_u32_e32 v63, vcc, 0, v59, vcc
	global_load_dwordx4 v[58:61], v[60:61], off nt
	s_nop 0
	global_load_dwordx4 v[62:65], v[62:63], off nt
	s_branch .LBB0_999

.LBB0_1311:
	s_lshl_b32 s0, s82, 2
	s_add_i32 s0, s0, s92
	s_add_i32 s0, s0, -4
	s_cmpk_gt_u32 s1, 0xff
	s_cselect_b32 s14, s0, -1
	s_cmp_lt_i32 s14, 0
	s_cbranch_scc1 .LBB0_1329
	s_cmpk_gt_u32 s88, 0xe0
	s_mov_b32 s0, 0x10000
	s_cselect_b32 s0, s0, 0x16000
	s_cmpk_gt_i32 s88, 0xab
	s_cselect_b32 s1, 0x9000, 0
	s_cselect_b32 s18, s0, 0x18000
	s_add_i32 s19, s14, s1
	s_cmp_ge_u32 s19, s18
	s_cbranch_scc1 .LBB0_1329
	s_load_dwordx2 s[4:5], s[90:91], 0xa0
	s_load_dwordx2 s[6:7], s[90:91], 0xb0
	s_load_dwordx2 s[8:9], s[90:91], 0xc0
	s_cmpk_gt_u32 s19, 0xffff
	v_readfirstlane_b32 s34, v0
	s_waitcnt vmcnt(0)
	v_lshlrev_b32_e32 v2, 2, v1
	s_cbranch_scc0 .LBB0_1315
	s_add_i32 s34, s19, 0xffff0000
	s_lshr_b32 s0, s34, 10
	s_mov_b32 s1, 0
	s_lshl_b64 s[0:1], s[0:1], 24
	s_waitcnt lgkmcnt(0)
	s_add_u32 s10, s8, s0
	s_addc_u32 s11, s9, s1
	s_lshl_b32 s1, s19, 6
	s_lshl_b32 s0, s19, 1
	s_and_b32 s1, s1, 0x7c0
	v_and_b32_e32 v142, 60, v2
	v_or_b32_e32 v130, s1, v142
	v_mov_b32_e32 v143, s0
	v_mov_b32_e32 v3, v143
	s_cbranch_execz .LBB0_1316
	s_branch .LBB0_1317
